# stack + bank-conflict-free 16B-slot XOR swizzle (row bits 2^3) for the mLSTM scan's Q/K/C^T LDS images (all readers and writers)
# speedup vs baseline: 1.0179x; 1.0052x over previous
.LBB0_409:
	s_mul_i32 s1, s10, 0x2200000
	v_readlane_b32 s6, v255, 11
	s_mul_hi_i32 s0, s10, 0x2200000
	s_add_u32 s6, s6, s1
	v_readlane_b32 s1, v255, 12
	s_addc_u32 s7, s1, s0
	s_lshl_b32 s42, s12, 1
	s_add_u32 s0, s16, s42
	s_addc_u32 s1, s17, 0
	s_lshl_b32 s12, s44, 3
	v_readlane_b32 s13, v255, 1
	s_add_i32 s28, s12, s13
	s_add_u32 s12, s6, s42
	s_addc_u32 s13, s7, 0
	s_lshl_b32 s6, s10, 3
	s_ashr_i32 s7, s6, 31
	s_lshl_b32 s48, s9, 12
	s_lshl_b64 s[6:7], s[6:7], 2
	v_readlane_b32 s14, v255, 9
	v_readlane_b32 s15, v255, 10
	s_add_u32 s6, s14, s6
	s_addc_u32 s7, s15, s7
	s_lshl_b32 s8, s8, 2
	s_add_u32 s6, s6, s8
	v_lshlrev_b32_e32 v3, 4, v1
	s_addc_u32 s7, s7, 0
	v_and_b32_e32 v7, 0x70, v3
	v_readlane_b32 s29, v255, 24
	v_and_b32_e32 v13, 48, v3
	v_writelane_b32 v255, s6, 32
	v_and_b32_e32 v3, 3, v1
	v_and_b32_e32 v5, 15, v1
	v_writelane_b32 v255, s7, 33
	v_cmp_eq_u32_e64 s[6:7], 0, v3
	v_readlane_b32 s9, v255, 28
	s_movk_i32 s18, 0x210
	v_writelane_b32 v255, s6, 34
	v_lshlrev_b32_e32 v14, 4, v3
	s_lshl_b32 s10, s11, 5
	v_writelane_b32 v255, s7, 35
	v_mul_lo_u32 v4, v124, s18
	v_readlane_b32 s6, v255, 18
	v_readlane_b32 s8, v255, 16
	s_movk_i32 s30, 0x50
	v_or_b32_e32 v130, s6, v5
	v_mul_lo_u32 v3, v130, s18
	s_movk_i32 s6, 0x90
	v_add_u32_e32 v15, 0, v3
	v_mul_lo_u32 v3, v130, s6
	v_readlane_b32 s6, v255, 29
	v_lshrrev_b32_e32 v2, 4, v123
	v_add_u32_e32 v9, 0, v4
	v_add_u32_e32 v133, s6, v3
	v_or_b32_e32 v3, s8, v5
	v_mul_u32_u24_e32 v134, 0x210, v3
	v_lshlrev_b32_e32 v3, 2, v1
	s_lshl_b32 s6, s11, 6
	v_and_b32_e32 v3, 12, v3
	s_add_u32 s6, s12, s6
	v_or_b32_e32 v10, s8, v3
	s_addc_u32 s7, s13, 0
	s_lshl_b32 s8, s8, 1
	v_mul_lo_u32 v4, v125, s30
	s_add_u32 s6, s6, s8
	v_add_u32_e32 v11, s29, v4
	v_add_u32_e32 v129, s9, v4
	v_lshlrev_b32_e32 v4, 2, v2
	v_lshlrev_b32_e32 v2, 3, v2
	v_lshlrev_b32_e32 v137, 1, v3
	s_addc_u32 s7, s7, 0
	v_mov_b32_e32 v3, v107
	v_lshl_add_u64 v[110:111], s[6:7], 0, v[2:3]
	v_readlane_b32 s6, v255, 17
	v_readlane_b32 s14, v255, 19
	v_lshrrev_b32_e32 v128, 5, v123
	v_lshrrev_b32_e32 v250, 3, v123
	v_and_b32_e32 v251, 7, v123
	v_lshlrev_b32_e32 v252, 16, v250
	v_lshlrev_b32_e32 v253, 4, v250
	v_lshl_or_b32 v250, v251, 4, v252
	v_lshl_or_b32 v251, v251, 9, v253
	v_add_u32_e32 v17, s6, v8
	v_readlane_b32 s6, v255, 20
	v_or_b32_e32 v132, s14, v4
	v_and_b32_e32 v108, 31, v1
	v_or_b32_e32 v4, s6, v4
	v_cmp_eq_u32_e64 s[6:7], 0, v123
	v_and_b32_e32 v131, 48, v1
	v_bfe_u32 v6, v1, 2, 2
	v_writelane_b32 v255, s6, 36
	v_lshlrev_b32_e32 v136, 1, v10
	v_and_b32_e32 v10, 32, v1
	v_writelane_b32 v255, s7, 37
	s_and_b32 s6, s28, 0x7c0
	v_or_b32_e32 v1, s6, v128
	v_cmp_gt_u32_e64 s[6:7], v132, v130
	v_lshlrev_b32_e32 v12, 11, v1
	v_or_b32_e32 v1, s14, v5
	v_writelane_b32 v255, s6, 38
	v_lshl_add_u64 v[112:113], s[0:1], 0, v[106:107]
	v_mul_u32_u24_e32 v19, 0x210, v1
	v_writelane_b32 v255, s7, 39
	v_or_b32_e32 v1, 2, v132
	v_readlane_b32 s0, v255, 23
	v_or_b32_e32 v21, 17, v132
	v_cmp_gt_u32_e64 s[16:17], v1, v130
	v_lshl_add_u32 v140, v4, 1, s0
	s_lshl_b32 s0, s10, 1
	v_or_b32_e32 v1, 3, v132
	v_cmp_gt_u32_e64 s[22:23], v21, v130
	v_or_b32_e32 v21, 18, v132
	v_writelane_b32 v255, s0, 40
	v_or_b32_e32 v3, v2, v6
	v_cmp_gt_u32_e64 s[18:19], v1, v130
	v_or_b32_e32 v1, 16, v132
	v_cmp_gt_u32_e64 s[24:25], v21, v130
	v_or_b32_e32 v21, 19, v132
	v_or_b32_e32 v2, 32, v2
	v_writelane_b32 v255, s1, 41
	v_mul_u32_u24_e32 v135, 0x210, v5
	v_add_u32_e32 v16, s9, v8
	v_cmp_eq_u32_e64 s[8:9], 0, v5
	v_add_u32_e32 v18, 0, v131
	v_lshlrev_b32_e32 v20, 1, v132
	v_cmp_gt_u32_e64 s[20:21], v1, v130
	v_cmp_gt_u32_e64 s[26:27], v21, v130
	v_lshlrev_b32_e32 v21, 1, v1
	v_mul_u32_u24_e32 v22, 0x50, v3
	v_mov_b32_e32 v1, s29
	v_lshlrev_b32_e32 v23, 1, v2
	v_or_b32_e32 v2, v2, v6
	v_mul_u32_u24_e32 v24, 0x210, v3
	v_mov_b32_e32 v66, 0
	v_and_or_b32 v5, v122, 64, v5
	v_writelane_b32 v255, s51, 42
	s_mov_b32 s49, 0
	v_cmp_lt_u32_e64 s[14:15], v132, v130
	v_mad_u32_u24 v138, v3, s30, v1
	v_mad_u32_u24 v139, v2, s30, v1
	s_bfe_u32 s50, s28, 0x50006
	v_mov_b32_e32 v2, v107
	v_mov_b32_e32 v1, v107
	v_mov_b32_e32 v4, v107
	v_mov_b32_e32 v3, v107
	v_mov_b32_e32 v6, v107
	v_add_u32_e32 v141, v9, v7
	v_add_u32_e32 v142, v11, v13
	v_lshlrev_b32_e32 v114, 1, v8
	v_lshlrev_b32_e32 v116, 2, v12
	v_lshlrev_b32_e32 v106, 2, v108
	v_add_u32_e32 v143, v129, v14
	v_add_u32_e32 v144, v133, v20
	v_add_u32_e32 v145, v133, v21
	v_add_u32_e32 v146, v133, v23
	v_add_u32_e32 v147, v16, v22
	v_add_u32_e32 v148, v17, v24
	v_lshlrev_b32_e32 v118, 1, v10
	v_add_u32_e32 v149, v15, v131
	v_add_u32_e32 v150, v18, v19
	v_lshlrev_b32_e32 v151, 2, v5
	v_writelane_b32 v255, s46, 43
	s_mov_b32 s47, 0
	s_mov_b32 s6, 0
	s_mov_b32 s7, 0
	v_mov_b32_e32 v67, v66
	v_mov_b32_e32 v68, v66
	v_mov_b32_e32 v69, v66
	v_mov_b32_e32 v70, v66
	v_mov_b32_e32 v71, v66
	v_mov_b32_e32 v72, v66
	v_mov_b32_e32 v73, v66
	v_mov_b32_e32 v78, v66
	v_mov_b32_e32 v79, v66
	v_mov_b32_e32 v80, v66
	v_mov_b32_e32 v81, v66
	v_mov_b32_e32 v74, v66
	v_mov_b32_e32 v75, v66
	v_mov_b32_e32 v76, v66
	v_mov_b32_e32 v77, v66
	v_mov_b32_e32 v82, v66
	v_mov_b32_e32 v83, v66
	v_mov_b32_e32 v84, v66
	v_mov_b32_e32 v85, v66
	v_mov_b32_e32 v86, v66
	v_mov_b32_e32 v87, v66
	v_mov_b32_e32 v88, v66
	v_mov_b32_e32 v89, v66
	v_mov_b32_e32 v5, v107
	v_mov_b32_e32 v8, v107
	v_mov_b32_e32 v7, v107
	v_mov_b32_e32 v10, v107
	v_mov_b32_e32 v9, v107
	v_mov_b32_e32 v12, v107
	v_mov_b32_e32 v11, v107
	v_mov_b32_e32 v14, v107
	v_mov_b32_e32 v13, v107
	v_mov_b32_e32 v16, v107
	v_mov_b32_e32 v15, v107
	v_mov_b32_e32 v18, v107
	v_mov_b32_e32 v17, v107
	v_mov_b32_e32 v20, v107
	v_mov_b32_e32 v19, v107
	v_mov_b32_e32 v22, v107
	v_mov_b32_e32 v21, v107
	v_mov_b32_e32 v24, v107
	v_mov_b32_e32 v23, v107
	v_mov_b32_e32 v26, v107
	v_mov_b32_e32 v25, v107
	v_mov_b32_e32 v28, v107
	v_mov_b32_e32 v27, v107
	v_mov_b32_e32 v30, v107
	v_mov_b32_e32 v29, v107
	v_mov_b32_e32 v32, v107
	v_mov_b32_e32 v31, v107
	v_lshrrev_b32_e32 v33, 2, v222
	v_lshrrev_b32_e32 v30, 3, v222
	v_xor_b32_e32 v33, v33, v30
	v_and_b32_e32 v33, 1, v33
	v_mov_b32_e32 v32, v131
	v_lshlrev_b32_e32 v30, 4, v33
	v_xor_b32_e32 v131, v131, v30
	v_sub_u32_e32 v30, v131, v32
	v_add_u32_e32 v149, v149, v30
	v_add_u32_e32 v150, v150, v30
	v_bfe_u32 v31, v222, 5, 1
	v_xor_b32_e32 v30, v31, v33
	v_sub_u32_e32 v31, v30, v31
	v_lshlrev_b32_e32 v31, 4, v31
	v_lshrrev_b32_e32 v30, 5, v0
	v_lshrrev_b32_e32 v33, 6, v0
	v_xor_b32_e32 v30, v30, v33
	v_and_b32_e32 v30, 1, v30
	v_and_b32_e32 v33, 1, v0
	v_xor_b32_e32 v30, v30, v33
	v_sub_u32_e32 v30, v30, v33
	v_lshlrev_b32_e32 v30, 4, v30
	v_add_u32_e32 v141, v141, v30
	v_bfe_u32 v33, v222, 1, 1
	v_bfe_u32 v30, v222, 4, 1
	v_xor_b32_e32 v30, v30, v33
	v_sub_u32_e32 v106, v30, v33
	v_lshlrev_b32_e32 v106, 4, v106
	v_xor_b32_e32 v30, 1, v30
	v_sub_u32_e32 v30, v30, v33
	v_lshlrev_b32_e32 v30, 4, v30
	v_add_u32_e32 v30, v148, v30
	v_add_u32_e32 v148, v148, v106
	s_waitcnt vmcnt(0)
	s_branch .LBB0_411

.Lqk_done:
.LBB0_447:
	v_lshl_add_u32 v184, v132, 2, s60
	s_waitcnt lgkmcnt(0)
	ds_read_b128 v[102:105], v184
	v_readlane_b32 s28, v255, 38
	v_readlane_b32 s29, v255, 39
	s_waitcnt lgkmcnt(0)
	v_sub_f32_e32 v102, v102, v183
	v_mul_f32_e32 v102, 0x3fb8aa3b, v102
	v_exp_f32_e32 v102, v102
	v_sub_f32_e32 v103, v103, v183
	v_sub_f32_e32 v104, v104, v183
	v_mul_f32_e32 v103, 0x3fb8aa3b, v103
	v_mul_f32_e32 v98, v98, v102
	v_sub_f32_e32 v102, v105, v183
	v_exp_f32_e32 v103, v103
	v_mul_f32_e32 v104, 0x3fb8aa3b, v104
	v_mul_f32_e32 v102, 0x3fb8aa3b, v102
	v_exp_f32_e32 v104, v104
	v_exp_f32_e32 v102, v102
	v_mul_f32_e32 v99, v99, v103
	v_cndmask_b32_e64 v98, v98, 0, s[28:29]
	v_cndmask_b32_e64 v99, 0, v99, s[14:15]
	v_mul_f32_e32 v100, v100, v104
	v_mul_f32_e32 v101, v101, v102
	v_cndmask_b32_e64 v100, v100, 0, s[16:17]
	v_cndmask_b32_e64 v101, v101, 0, s[18:19]
	v_cvt_pk_bf16_f32 v98, v98, v99
	v_cvt_pk_bf16_f32 v99, v100, v101
	ds_write_b64 v144, v[98:99]
	ds_read_b128 v[98:101], v184 offset:64
	s_mul_i32 s28, s6, 0x4620
	s_add_i32 s28, s28, 0
	s_add_i32 s28, s28, 0x10800
	s_waitcnt lgkmcnt(0)
	v_sub_f32_e32 v98, v98, v183
	v_sub_f32_e32 v99, v99, v183
	v_mul_f32_e32 v98, 0x3fb8aa3b, v98
	v_mul_f32_e32 v99, 0x3fb8aa3b, v99
	v_exp_f32_e32 v98, v98
	v_exp_f32_e32 v99, v99
	v_mul_f32_e32 v94, v94, v98
	v_mul_f32_e32 v95, v95, v99
	v_sub_f32_e32 v98, v100, v183
	v_sub_f32_e32 v99, v101, v183
	v_mul_f32_e32 v98, 0x3fb8aa3b, v98
	v_mul_f32_e32 v99, 0x3fb8aa3b, v99
	v_exp_f32_e32 v98, v98
	v_exp_f32_e32 v99, v99
	v_cndmask_b32_e64 v94, v94, 0, s[20:21]
	v_cndmask_b32_e64 v95, v95, 0, s[22:23]
	v_mul_f32_e32 v96, v96, v98
	v_mul_f32_e32 v97, v97, v99
	v_cndmask_b32_e64 v96, v96, 0, s[24:25]
	v_cndmask_b32_e64 v97, v97, 0, s[26:27]
	v_cvt_pk_bf16_f32 v94, v94, v95
	v_cvt_pk_bf16_f32 v95, v96, v97
	ds_write_b64 v145, v[94:95]
	s_waitcnt lgkmcnt(0)
	s_barrier
	v_add3_u32 v183, s28, v135, v131
	ds_read_b128 v[94:97], v183 offset:16896
	ds_read_b128 v[98:101], v149
	ds_read_b128 v[102:105], v183 offset:16960
	ds_read_b128 v[184:187], v149 offset:64
	s_waitcnt lgkmcnt(2)
	v_mfma_f32_16x16x32_bf16 v[94:97], v[94:97], v[98:101], 0
	ds_read_b128 v[188:191], v183 offset:17024
	ds_read_b128 v[192:195], v149 offset:128
	s_waitcnt lgkmcnt(2)
	v_mfma_f32_16x16x32_bf16 v[94:97], v[102:105], v[184:187], v[94:97]
	ds_read_b128 v[102:105], v183 offset:17088
	ds_read_b128 v[200:203], v149 offset:192
	s_waitcnt lgkmcnt(2)
	v_mfma_f32_16x16x32_bf16 v[94:97], v[188:191], v[192:195], v[94:97]
	ds_read_b128 v[188:191], v183 offset:17152
	ds_read_b128 v[204:207], v149 offset:256
	s_waitcnt lgkmcnt(2)
	v_mfma_f32_16x16x32_bf16 v[94:97], v[102:105], v[200:203], v[94:97]
	ds_read_b128 v[102:105], v183 offset:17216
	ds_read_b128 v[208:211], v149 offset:320
	s_waitcnt lgkmcnt(2)
	v_mfma_f32_16x16x32_bf16 v[94:97], v[188:191], v[204:207], v[94:97]
	ds_read_b128 v[188:191], v183 offset:17280
	ds_read_b128 v[212:215], v149 offset:384
	s_waitcnt lgkmcnt(2)
	v_mfma_f32_16x16x32_bf16 v[94:97], v[102:105], v[208:211], v[94:97]
	ds_read_b128 v[102:105], v183 offset:17344
	ds_read_b128 v[216:219], v149 offset:448
	v_add_u32_e32 v183, v133, v32
	s_waitcnt lgkmcnt(2)
	v_mfma_f32_16x16x32_bf16 v[94:97], v[188:191], v[212:215], v[94:97]
	v_add_u32_e32 v188, v138, v136
	ds_read_b64_tr_b16 v[190:191], v188 offset:320
	ds_read_b64_tr_b16 v[188:189], v188
	ds_read_b128 v[224:227], v183
	s_waitcnt lgkmcnt(3)
	v_mfma_f32_16x16x32_bf16 v[94:97], v[102:105], v[216:219], v[94:97]
	s_waitcnt lgkmcnt(0)
	v_mfma_f32_16x16x32_bf16 v[188:191], v[188:191], v[224:227], 0
	s_nop 5
	v_add_u32_e32 v95, v138, v137
	ds_read_b64_tr_b16 v[102:103], v95 offset:64
	ds_read_b64_tr_b16 v[104:105], v95 offset:384
	v_add_u32_e32 v95, v139, v136
	ds_read_b64_tr_b16 v[230:231], v95 offset:320
	ds_read_b64_tr_b16 v[228:229], v95
	ds_read_b128 v[232:235], v146
	v_add_u32_e32 v95, v139, v137
	s_waitcnt lgkmcnt(3)
	v_mfma_f32_16x16x32_bf16 v[102:105], v[102:105], v[224:227], 0
	ds_read_b64_tr_b16 v[224:225], v95 offset:64
	ds_read_b64_tr_b16 v[226:227], v95 offset:384
	v_add3_u32 v95, s28, v134, v131
	s_waitcnt lgkmcnt(2)
	v_mfma_f32_16x16x32_bf16 v[188:191], v[228:231], v[232:235], v[188:191]
	ds_read_b128 v[228:231], v95
	s_waitcnt lgkmcnt(1)
	v_mfma_f32_16x16x32_bf16 v[102:105], v[224:227], v[232:235], v[102:105]
	ds_read_b128 v[224:227], v95 offset:64
	s_waitcnt lgkmcnt(1)
	v_mfma_f32_16x16x32_bf16 v[96:99], v[228:231], v[98:101], 0
	ds_read_b128 v[228:231], v95 offset:128
	s_waitcnt lgkmcnt(1)
	v_mfma_f32_16x16x32_bf16 v[96:99], v[224:227], v[184:187], v[96:99]
	ds_read_b128 v[184:187], v95 offset:192
	s_waitcnt lgkmcnt(1)
	v_mfma_f32_16x16x32_bf16 v[96:99], v[228:231], v[192:195], v[96:99]
	ds_read_b128 v[192:195], v95 offset:256
	s_waitcnt lgkmcnt(1)
	v_mfma_f32_16x16x32_bf16 v[96:99], v[184:187], v[200:203], v[96:99]
	ds_read_b128 v[184:187], v95 offset:320
	s_waitcnt lgkmcnt(1)
	v_mfma_f32_16x16x32_bf16 v[96:99], v[192:195], v[204:207], v[96:99]
	ds_read2st64_b32 v[104:105], v182 offset0:2 offset1:3
	ds_read_b128 v[192:195], v95 offset:384
	s_waitcnt lgkmcnt(1)
	v_fmac_f32_e32 v102, v94, v104
	ds_bpermute_b32 v182, v151, v102
	v_mfma_f32_16x16x32_bf16 v[96:99], v[184:187], v[208:211], v[96:99]
	ds_read_b128 v[100:103], v95 offset:448
	s_waitcnt lgkmcnt(2)
	v_mfma_f32_16x16x32_bf16 v[94:97], v[192:195], v[212:215], v[96:99]
	s_waitcnt lgkmcnt(0)
	v_mfma_f32_16x16x32_bf16 v[94:97], v[100:103], v[216:219], v[94:97]
	s_nop 2
	v_max_f32_e64 v98, |v182|, |v182|
	v_max_f32_e32 v99, v105, v105
	v_max_f32_e32 v98, v98, v99
	v_div_scale_f32 v99, s[28:29], v98, v98, 1.0
	v_rcp_f32_e32 v105, v99
	v_fma_f32 v94, v94, v104, v188
	v_fma_f32 v95, v95, v104, v189
	v_fma_f32 v96, v96, v104, v190
	v_fma_f32 v100, -v99, v105, 1.0
	v_fmac_f32_e32 v105, v100, v105
	v_div_scale_f32 v100, vcc, 1.0, v98, 1.0
	v_mul_f32_e32 v101, v100, v105
	v_fma_f32 v102, -v99, v101, v100
	v_fmac_f32_e32 v101, v102, v105
	v_fma_f32 v99, -v99, v101, v100
	v_div_fmas_f32 v99, v99, v105, v101
	v_div_fixup_f32 v98, v99, v98, 1.0
	v_fmac_f32_e32 v191, v97, v104
	v_mov_b32_e32 v182, s60
	v_mul_f32_e32 v94, v94, v98
	v_mul_f32_e32 v95, v95, v98
	v_mul_f32_e32 v96, v96, v98
	v_mul_f32_e32 v97, v191, v98
	v_cvt_pk_bf16_f32 v200, v94, v95
	v_cvt_pk_bf16_f32 v201, v96, v97
	ds_read_b32 v196, v182 offset:1280
	ds_read_b64_tr_b16 v[94:95], v147
	ds_read_b64_tr_b16 v[98:99], v147 offset:32
	ds_read_b64_tr_b16 v[102:103], v147 offset:64
	ds_read_b64_tr_b16 v[184:185], v30 offset:35904
	ds_read_b64_tr_b16 v[182:183], v148 offset:33792
	ds_read_b64_tr_b16 v[96:97], v147 offset:320
	ds_read_b64_tr_b16 v[100:101], v147 offset:352
	ds_read_b64_tr_b16 v[104:105], v147 offset:384
	ds_read_b64_tr_b16 v[186:187], v147 offset:2560
	ds_read_b64_tr_b16 v[188:189], v148 offset:33824
	ds_read_b64_tr_b16 v[192:193], v147 offset:2944
	ds_read_b64_tr_b16 v[190:191], v30 offset:35936
	s_waitcnt lgkmcnt(12)
	v_pk_mul_f32 v[88:89], v[88:89], v[196:197] op_sel_hi:[1,0]
	v_pk_mul_f32 v[86:87], v[86:87], v[196:197] op_sel_hi:[1,0]
	v_pk_mul_f32 v[84:85], v[84:85], v[196:197] op_sel_hi:[1,0]
	v_pk_mul_f32 v[82:83], v[82:83], v[196:197] op_sel_hi:[1,0]
	v_pk_mul_f32 v[76:77], v[76:77], v[196:197] op_sel_hi:[1,0]
	v_pk_mul_f32 v[74:75], v[74:75], v[196:197] op_sel_hi:[1,0]
	v_pk_mul_f32 v[80:81], v[80:81], v[196:197] op_sel_hi:[1,0]
	v_pk_mul_f32 v[78:79], v[78:79], v[196:197] op_sel_hi:[1,0]
	v_pk_mul_f32 v[72:73], v[72:73], v[196:197] op_sel_hi:[1,0]
	v_pk_mul_f32 v[70:71], v[70:71], v[196:197] op_sel_hi:[1,0]
	v_pk_mul_f32 v[68:69], v[68:69], v[196:197] op_sel_hi:[1,0]
	v_pk_mul_f32 v[66:67], v[66:67], v[196:197] op_sel_hi:[1,0]
	s_waitcnt lgkmcnt(6)
	v_mfma_f32_16x16x32_bf16 v[86:89], v[182:185], v[94:97], v[86:89]
	s_add_i32 s28, s47, 0xffffff00
	s_cmp_lt_u32 s7, 4
	s_cselect_b32 s7, s47, s28
	s_waitcnt lgkmcnt(5)
	v_mfma_f32_16x16x32_bf16 v[82:85], v[182:185], v[98:101], v[82:85]
	s_waitcnt lgkmcnt(4)
	v_mfma_f32_16x16x32_bf16 v[74:77], v[182:185], v[102:105], v[74:77]
	ds_read_b64_tr_b16 v[182:183], v148 offset:50688
	ds_read_b64_tr_b16 v[194:195], v148 offset:50720
	ds_read_b64_tr_b16 v[184:185], v30 offset:52800
	s_waitcnt lgkmcnt(3)
	v_mfma_f32_16x16x32_bf16 v[78:81], v[188:191], v[94:97], v[78:81]
	v_mfma_f32_16x16x32_bf16 v[70:73], v[188:191], v[98:101], v[70:73]
	v_add_u32_e32 v98, s7, v130
	s_movk_i32 s7, 0xfff
	s_cselect_b32 s7, 0xff, s7
	v_mfma_f32_16x16x32_bf16 v[66:69], v[188:191], v[102:105], v[66:69]
	ds_read_b64_tr_b16 v[188:189], v147 offset:2880
	ds_read_b64_tr_b16 v[96:97], v147 offset:2912
	ds_read_b64_tr_b16 v[190:191], v147 offset:2624
	ds_read_b64_tr_b16 v[94:95], v147 offset:2592
	ds_read_b64_tr_b16 v[196:197], v30 offset:52832
	v_sub_u32_e32 v99, s7, v98
	v_cndmask_b32_e64 v98, v99, v98, s[2:3]
	s_cselect_b32 s7, s45, s48
	v_add_u32_e32 v98, s7, v98
	v_ashrrev_i32_e32 v99, 31, v98
	s_waitcnt lgkmcnt(4)
	v_mfma_f32_16x16x32_bf16 v[86:89], v[182:185], v[186:189], v[86:89]
	s_xor_b32 s6, s6, 1
	s_mul_i32 s7, s6, 0x4620
	s_waitcnt lgkmcnt(1)
	v_mfma_f32_16x16x32_bf16 v[82:85], v[182:185], v[94:97], v[82:85]
	v_mfma_f32_16x16x32_bf16 v[74:77], v[182:185], v[190:193], v[74:77]
	s_waitcnt lgkmcnt(0)
	v_mfma_f32_16x16x32_bf16 v[78:81], v[194:197], v[186:189], v[78:81]
	v_mfma_f32_16x16x32_bf16 v[70:73], v[194:197], v[94:97], v[70:73]
	v_lshlrev_b64 v[94:95], 11, v[98:99]
	v_lshl_add_u64 v[94:95], v[110:111], 0, v[94:95]
	global_store_dwordx2 v[94:95], v[200:201], off
	v_mfma_f32_16x16x32_bf16 v[66:69], v[194:197], v[190:193], v[66:69]
	v_add_u32_e32 v94, s7, v140
	v_cvt_pk_bf16_f32 v96, v86, v87
	v_cvt_pk_bf16_f32 v97, v88, v89
	v_add3_u32 v95, v94, v135, v31
	ds_write_b64 v95, v[96:97]
	v_cvt_pk_bf16_f32 v96, v82, v83
	v_cvt_pk_bf16_f32 v97, v84, v85
	ds_write_b64 v95, v[96:97] offset:8448
	s_and_saveexec_b64 s[28:29], s[8:9]
	s_cbranch_execz .LBB0_449
	v_cvt_pk_bf16_f32 v96, v74, v75
	v_cvt_pk_bf16_f32 v97, v76, v77
	ds_write_b64 v94, v[96:97] offset:16896
